# v9 + a second w_down sjob per wave in each gate_up epilogue (first/second half), streaming K-loop trips only in units 1-2
# speedup vs baseline: 1.0218x; 1.0090x over previous
; __device__ __forceinline__ unsigned pk4_fp8(float a, float b, float c, float d) { int p = __builtin_amdgcn_cvt_pk_fp8_f32(a, b, 0, false); p = __builtin_amdgcn_cvt_pk_fp8_f32(c, d, p, true); return (unsigned)p; }
;     __device__ __forceinline__ void operator()(const f32x4 (&acc)[2][2][4][2], const Unit& u, int wr, int wc, int fr, int fq) const {
;         const int row0 = u.pm * BM + wr * 64 + fr, cc = u.pn * HALF + wc * 32 + 8 * fq;
;         const float* bp = bias + (size_t)u.e * 4096 + cc;
;         f32x4 bg[2], bu[2];
; #pragma unroll
;         for (int n = 0; n < 2; ++n) { bg[n] = *(const f32x4*)(bp + 4 * n); bu[n] = *(const f32x4*)(bp + 2048 + 4 * n); }
; #pragma unroll
;         for (int ai = 0; ai < 2; ++ai)
; #pragma unroll
;             for (int m = 0; m < 4; ++m) { float r[8];
; #pragma unroll
;                 for (int n = 0; n < 2; ++n)
; #pragma unroll
;                     for (int j = 0; j < 4; ++j) {
;                         float g = acc[ai][0][m][n][j] * W8_INV + bg[n][j], uu = acc[ai][1][m][n][j] * W8_INV + bu[n][j];
;                         g = fminf(g, 7.0f); uu = fminf(fmaxf(uu, -7.0f), 7.0f);
;                         const float glu = g * __builtin_amdgcn_rcpf(1.0f + __expf(-1.702f * g));
;                         r[n * 4 + j] = (uu + 1.0f) * glu; }
;                 u32x2 w; w.x = pk4_fp8(r[0], r[1], r[2], r[3]); w.y = pk4_fp8(r[4], r[5], r[6], r[7]);
;                 *(u32x2*)(O + (size_t)(row0 + ai * HALF + m * 16) * DM + cc) = w; }
.Lesj_join:
	v_fmamk_f32 v19, v175, 0x3c800000, v15
	v_fmamk_f32 v25, v166, 0x3c800000, v6
	v_min_f32_e32 v19, 0x40e00000, v19
	v_min_f32_e32 v25, 0x40e00000, v25
	v_fmamk_f32 v23, v176, 0x3c800000, v16
	v_mul_f32_e32 v36, 0xbfd9db23, v19
	v_mul_f32_e32 v39, 0xbfd9db23, v25
	v_min_f32_e32 v23, 0x40e00000, v23
	v_mul_f32_e32 v36, 0x3fb8aa3b, v36
	v_mul_f32_e32 v39, 0x3fb8aa3b, v39
	v_mul_f32_e32 v37, 0xbfd9db23, v23
	v_exp_f32_e32 v36, v36
	v_exp_f32_e32 v39, v39
	v_mul_f32_e32 v37, 0x3fb8aa3b, v37
	v_fmamk_f32 v18, v174, 0x3c800000, v14
	v_fmamk_f32 v24, v177, 0x3c800000, v17
	v_exp_f32_e32 v37, v37
	v_min_f32_e32 v18, 0x40e00000, v18
	v_min_f32_e32 v24, 0x40e00000, v24
	v_mul_f32_e32 v35, 0xbfd9db23, v18
	v_mul_f32_e32 v38, 0xbfd9db23, v24
	v_add_f32_e32 v36, 1.0, v36
	v_add_f32_e32 v39, 1.0, v39
	v_mul_f32_e32 v35, 0x3fb8aa3b, v35
	v_mul_f32_e32 v38, 0x3fb8aa3b, v38
	v_rcp_f32_e32 v36, v36
	v_rcp_f32_e32 v39, v39
	v_exp_f32_e32 v35, v35
	v_exp_f32_e32 v38, v38
	v_add_f32_e32 v37, 1.0, v37
	v_fmamk_f32 v27, v168, 0x3c800000, v8
	v_fmamk_f32 v29, v171, 0x3c800000, v11
	v_fmamk_f32 v32, v162, 0x3c800000, v2
	v_rcp_f32_e32 v37, v37
	v_min_f32_e32 v27, 0x40e00000, v27
	v_med3_f32 v29, v29, s57, v196
	v_med3_f32 v32, v32, s57, v196
	v_fmamk_f32 v26, v167, 0x3c800000, v7
	v_fmamk_f32 v30, v172, 0x3c800000, v12
	v_mul_f32_e32 v41, 0xbfd9db23, v27
	v_add_f32_e32 v29, 1.0, v29
	v_add_f32_e32 v32, 1.0, v32
	v_mul_f32_e32 v19, v19, v36
	v_mul_f32_e32 v25, v25, v39
	v_min_f32_e32 v26, 0x40e00000, v26
	v_med3_f32 v30, v30, s57, v196
	v_mul_f32_e32 v41, 0x3fb8aa3b, v41
	v_add_f32_e32 v35, 1.0, v35
	v_add_f32_e32 v38, 1.0, v38
	v_mul_f32_e32 v19, v29, v19
	v_mul_f32_e32 v29, v32, v25
	v_fmamk_f32 v25, v169, 0x3c800000, v9
	v_mul_f32_e32 v40, 0xbfd9db23, v26
	v_add_f32_e32 v30, 1.0, v30
	v_exp_f32_e32 v41, v41
	v_rcp_f32_e32 v35, v35
	v_rcp_f32_e32 v38, v38
	v_mul_f32_e32 v23, v23, v37
	v_min_f32_e32 v25, 0x40e00000, v25
	v_mul_f32_e32 v40, 0x3fb8aa3b, v40
	v_mul_f32_e32 v23, v30, v23
	v_mul_f32_e32 v30, 0xbfd9db23, v25
	v_fmamk_f32 v28, v170, 0x3c800000, v10
	v_fmamk_f32 v31, v173, 0x3c800000, v13
	v_exp_f32_e32 v40, v40
	v_mul_f32_e32 v30, 0x3fb8aa3b, v30
	v_med3_f32 v28, v28, s57, v196
	v_med3_f32 v31, v31, s57, v196
	v_exp_f32_e32 v30, v30
	v_add_f32_e32 v28, 1.0, v28
	v_add_f32_e32 v31, 1.0, v31
	v_add_f32_e32 v41, 1.0, v41
	v_mul_f32_e32 v18, v18, v35
	v_mul_f32_e32 v24, v24, v38
	v_mul_f32_e32 v18, v28, v18
	v_mul_f32_e32 v28, v31, v24
	v_rcp_f32_e32 v24, v41
	v_add_f32_e32 v40, 1.0, v40
	v_fmamk_f32 v34, v164, 0x3c800000, v4
	v_rcp_f32_e32 v40, v40
	v_add_f32_e32 v30, 1.0, v30
	v_med3_f32 v31, v34, s57, v196
	v_rcp_f32_e32 v30, v30
	v_fmamk_f32 v33, v163, 0x3c800000, v3
	v_mul_f32_e32 v24, v27, v24
	v_add_f32_e32 v27, 1.0, v31
	v_med3_f32 v33, v33, s57, v196
	v_mul_f32_e32 v27, v27, v24
	v_fmamk_f32 v24, v165, 0x3c800000, v5
	v_add_f32_e32 v33, 1.0, v33
	v_mul_f32_e32 v26, v26, v40
	v_med3_f32 v31, v24, s57, v196
	v_mov_b32_e32 v24, v181
	v_mul_f32_e32 v26, v33, v26
	v_mul_f32_e32 v30, v25, v30
	v_cvt_pk_fp8_f32 v24, v18, v19
	v_mov_b32_e32 v25, v181
	v_cvt_pk_fp8_f32 v25, v29, v26
	v_add_f32_e32 v18, 1.0, v31
	v_mul_f32_e32 v18, v18, v30
	v_cvt_pk_fp8_f32 v24, v23, v28 op_sel:[0,0,1]
	v_ashrrev_i32_e32 v23, 31, v22
	v_cvt_pk_fp8_f32 v25, v27, v18 op_sel:[0,0,1]
	v_lshlrev_b64 v[18:19], 11, v[22:23]
	v_fmamk_f32 v23, v158, 0x3c800000, v14
	v_min_f32_e32 v23, 0x40e00000, v23
	v_mul_f32_e32 v26, 0xbfd9db23, v23
	v_mul_f32_e32 v26, 0x3fb8aa3b, v26
	v_exp_f32_e32 v26, v26
	v_lshl_add_u64 v[18:19], s[8:9], 0, v[18:19]
	v_lshl_add_u64 v[18:19], v[18:19], 0, v[20:21]
	global_store_dwordx2 v[18:19], v[24:25], off
	v_add_f32_e32 v25, 1.0, v26
	v_fmamk_f32 v26, v159, 0x3c800000, v15
	v_min_f32_e32 v26, 0x40e00000, v26
	v_mul_f32_e32 v27, 0xbfd9db23, v26
	v_mul_f32_e32 v27, 0x3fb8aa3b, v27
	v_rcp_f32_e32 v25, v25
	v_exp_f32_e32 v27, v27
	v_fmamk_f32 v28, v161, 0x3c800000, v17
	v_min_f32_e32 v28, 0x40e00000, v28
	v_mul_f32_e32 v23, v23, v25
	v_add_f32_e32 v25, 1.0, v27
	v_rcp_f32_e32 v25, v25
	v_mul_f32_e32 v29, 0xbfd9db23, v28
	v_mul_f32_e32 v29, 0x3fb8aa3b, v29
	v_exp_f32_e32 v29, v29
	v_mul_f32_e32 v25, v26, v25
	v_fmamk_f32 v26, v160, 0x3c800000, v16
	v_min_f32_e32 v26, 0x40e00000, v26
	v_mul_f32_e32 v27, 0xbfd9db23, v26
	v_mul_f32_e32 v27, 0x3fb8aa3b, v27
	v_exp_f32_e32 v27, v27
	v_fmamk_f32 v30, v151, 0x3c800000, v7
	v_min_f32_e32 v30, 0x40e00000, v30
	v_mul_f32_e32 v31, 0xbfd9db23, v30
	v_add_f32_e32 v27, 1.0, v27
	v_rcp_f32_e32 v27, v27
	v_mul_f32_e32 v31, 0x3fb8aa3b, v31
	v_exp_f32_e32 v31, v31
	v_fmamk_f32 v24, v154, 0x3c800000, v10
	v_mul_f32_e32 v26, v26, v27
	v_add_f32_e32 v27, 1.0, v29
	v_rcp_f32_e32 v27, v27
	v_med3_f32 v24, v24, s57, v196
	v_add_f32_e32 v24, 1.0, v24
	v_mul_f32_e32 v23, v24, v23
	v_mul_f32_e32 v27, v28, v27
	v_fmamk_f32 v28, v150, 0x3c800000, v6
	v_min_f32_e32 v28, 0x40e00000, v28
	v_mul_f32_e32 v29, 0xbfd9db23, v28
	v_mul_f32_e32 v29, 0x3fb8aa3b, v29
	v_exp_f32_e32 v29, v29
	v_fmamk_f32 v24, v155, 0x3c800000, v11
	v_med3_f32 v24, v24, s57, v196
	v_add_f32_e32 v24, 1.0, v24
	v_add_f32_e32 v29, 1.0, v29
	v_rcp_f32_e32 v29, v29
	v_mul_f32_e32 v25, v24, v25
	v_fmamk_f32 v24, v156, 0x3c800000, v12
	v_med3_f32 v24, v24, s57, v196
	v_mul_f32_e32 v28, v28, v29
	v_add_f32_e32 v29, 1.0, v31
	v_rcp_f32_e32 v29, v29
	v_add_f32_e32 v24, 1.0, v24
	v_mul_f32_e32 v26, v24, v26
	v_fmamk_f32 v24, v157, 0x3c800000, v13
	v_mul_f32_e32 v29, v30, v29
	v_fmamk_f32 v30, v152, 0x3c800000, v8
	v_min_f32_e32 v30, 0x40e00000, v30
	v_mul_f32_e32 v31, 0xbfd9db23, v30
	v_med3_f32 v24, v24, s57, v196
	v_mul_f32_e32 v31, 0x3fb8aa3b, v31
	v_add_f32_e32 v24, 1.0, v24
; __device__ __forceinline__ unsigned pk4_fp8(float a, float b, float c, float d) { int p = __builtin_amdgcn_cvt_pk_fp8_f32(a, b, 0, false); p = __builtin_amdgcn_cvt_pk_fp8_f32(c, d, p, true); return (unsigned)p; }
;     __device__ __forceinline__ void operator()(const f32x4 (&acc)[2][2][4][2], const Unit& u, int wr, int wc, int fr, int fq) const {
;     ...
;             for (int m = 0; m < 4; ++m) { float r[8];
; #pragma unroll
;                 for (int n = 0; n < 2; ++n)
; #pragma unroll
;                     for (int j = 0; j < 4; ++j) {
;                         float g = acc[ai][0][m][n][j] * W8_INV + bg[n][j], uu = acc[ai][1][m][n][j] * W8_INV + bu[n][j];
;                         g = fminf(g, 7.0f); uu = fminf(fmaxf(uu, -7.0f), 7.0f);
;                         const float glu = g * __builtin_amdgcn_rcpf(1.0f + __expf(-1.702f * g));
;                         r[n * 4 + j] = (uu + 1.0f) * glu; }
;                 u32x2 w; w.x = pk4_fp8(r[0], r[1], r[2], r[3]); w.y = pk4_fp8(r[4], r[5], r[6], r[7]);
;                 *(u32x2*)(O + (size_t)(row0 + ai * HALF + m * 16) * DM + cc) = w; }
	v_exp_f32_e32 v31, v31
	v_mul_f32_e32 v27, v24, v27
	v_fmamk_f32 v24, v146, 0x3c800000, v2
	v_med3_f32 v24, v24, s57, v196
	v_fmamk_f32 v32, v153, 0x3c800000, v9
	v_add_f32_e32 v24, 1.0, v24
	v_min_f32_e32 v32, 0x40e00000, v32
	v_mul_f32_e32 v28, v24, v28
	v_fmamk_f32 v24, v147, 0x3c800000, v3
	v_add_f32_e32 v31, 1.0, v31
	v_mul_f32_e32 v33, 0xbfd9db23, v32
	v_med3_f32 v24, v24, s57, v196
	v_rcp_f32_e32 v31, v31
	v_mul_f32_e32 v33, 0x3fb8aa3b, v33
	v_add_f32_e32 v24, 1.0, v24
	v_exp_f32_e32 v33, v33
	v_mul_f32_e32 v29, v24, v29
	v_fmamk_f32 v24, v148, 0x3c800000, v4
	v_med3_f32 v24, v24, s57, v196
	v_mul_f32_e32 v30, v30, v31
	v_add_f32_e32 v24, 1.0, v24
	v_add_f32_e32 v31, 1.0, v33
	v_mul_f32_e32 v30, v24, v30
	v_fmamk_f32 v24, v149, 0x3c800000, v5
	v_rcp_f32_e32 v31, v31
	v_med3_f32 v33, v24, s57, v196
	v_mov_b32_e32 v24, v181
	v_cvt_pk_fp8_f32 v24, v23, v25
	v_mov_b32_e32 v25, v181
	v_cvt_pk_fp8_f32 v25, v28, v29
	v_mul_f32_e32 v31, v32, v31
	v_add_f32_e32 v23, 1.0, v33
	v_mul_f32_e32 v23, v23, v31
	v_cvt_pk_fp8_f32 v24, v26, v27 op_sel:[0,0,1]
	v_cvt_pk_fp8_f32 v25, v30, v23 op_sel:[0,0,1]
	v_or_b32_e32 v26, 16, v22
	v_fmamk_f32 v23, v142, 0x3c800000, v14
	v_ashrrev_i32_e32 v27, 31, v26
	v_min_f32_e32 v23, 0x40e00000, v23
	v_lshlrev_b64 v[26:27], 11, v[26:27]
	v_mul_f32_e32 v28, 0xbfd9db23, v23
	v_lshl_add_u64 v[26:27], s[8:9], 0, v[26:27]
	v_mul_f32_e32 v28, 0x3fb8aa3b, v28
	v_exp_f32_e32 v28, v28
	v_lshl_add_u64 v[26:27], v[26:27], 0, v[20:21]
	global_store_dwordx2 v[26:27], v[24:25], off
	v_fmamk_f32 v26, v143, 0x3c800000, v15
	v_min_f32_e32 v26, 0x40e00000, v26
	v_mul_f32_e32 v27, 0xbfd9db23, v26
	v_add_f32_e32 v25, 1.0, v28
	v_mul_f32_e32 v27, 0x3fb8aa3b, v27
	v_rcp_f32_e32 v25, v25
	v_exp_f32_e32 v27, v27
	v_fmamk_f32 v28, v145, 0x3c800000, v17
	v_min_f32_e32 v28, 0x40e00000, v28
	v_mul_f32_e32 v23, v23, v25
	v_add_f32_e32 v25, 1.0, v27
	v_rcp_f32_e32 v25, v25
	v_mul_f32_e32 v29, 0xbfd9db23, v28
	v_mul_f32_e32 v29, 0x3fb8aa3b, v29
	v_exp_f32_e32 v29, v29
	v_mul_f32_e32 v25, v26, v25
	v_fmamk_f32 v26, v144, 0x3c800000, v16
	v_min_f32_e32 v26, 0x40e00000, v26
	v_mul_f32_e32 v27, 0xbfd9db23, v26
	v_mul_f32_e32 v27, 0x3fb8aa3b, v27
	v_exp_f32_e32 v27, v27
	v_fmamk_f32 v30, v135, 0x3c800000, v7
	v_min_f32_e32 v30, 0x40e00000, v30
	v_mul_f32_e32 v31, 0xbfd9db23, v30
	v_add_f32_e32 v27, 1.0, v27
	v_rcp_f32_e32 v27, v27
	v_mul_f32_e32 v31, 0x3fb8aa3b, v31
	v_exp_f32_e32 v31, v31
	v_fmamk_f32 v24, v138, 0x3c800000, v10
	v_mul_f32_e32 v26, v26, v27
	v_add_f32_e32 v27, 1.0, v29
	v_rcp_f32_e32 v27, v27
	v_med3_f32 v24, v24, s57, v196
	v_add_f32_e32 v24, 1.0, v24
	v_mul_f32_e32 v23, v24, v23
	v_mul_f32_e32 v27, v28, v27
	v_fmamk_f32 v28, v134, 0x3c800000, v6
	v_min_f32_e32 v28, 0x40e00000, v28
	v_mul_f32_e32 v29, 0xbfd9db23, v28
	v_mul_f32_e32 v29, 0x3fb8aa3b, v29
	v_exp_f32_e32 v29, v29
	v_fmamk_f32 v24, v139, 0x3c800000, v11
	v_med3_f32 v24, v24, s57, v196
	v_add_f32_e32 v24, 1.0, v24
	v_add_f32_e32 v29, 1.0, v29
	v_rcp_f32_e32 v29, v29
	v_mul_f32_e32 v25, v24, v25
	v_fmamk_f32 v24, v140, 0x3c800000, v12
	v_med3_f32 v24, v24, s57, v196
	v_mul_f32_e32 v28, v28, v29
	v_add_f32_e32 v29, 1.0, v31
	v_rcp_f32_e32 v29, v29
	v_add_f32_e32 v24, 1.0, v24
	v_mul_f32_e32 v26, v24, v26
	v_fmamk_f32 v24, v141, 0x3c800000, v13
	v_mul_f32_e32 v29, v30, v29
	v_fmamk_f32 v30, v136, 0x3c800000, v8
	v_min_f32_e32 v30, 0x40e00000, v30
	v_mul_f32_e32 v31, 0xbfd9db23, v30
	v_med3_f32 v24, v24, s57, v196
	v_mul_f32_e32 v31, 0x3fb8aa3b, v31
	v_add_f32_e32 v24, 1.0, v24
	v_exp_f32_e32 v31, v31
	v_mul_f32_e32 v27, v24, v27
	v_fmamk_f32 v24, v130, 0x3c800000, v2
	v_med3_f32 v24, v24, s57, v196
	v_fmamk_f32 v32, v137, 0x3c800000, v9
	v_add_f32_e32 v24, 1.0, v24
	v_min_f32_e32 v32, 0x40e00000, v32
	v_mul_f32_e32 v28, v24, v28
	v_fmamk_f32 v24, v131, 0x3c800000, v3
	v_add_f32_e32 v31, 1.0, v31
	v_mul_f32_e32 v33, 0xbfd9db23, v32
	v_med3_f32 v24, v24, s57, v196
	v_rcp_f32_e32 v31, v31
	v_mul_f32_e32 v33, 0x3fb8aa3b, v33
	v_add_f32_e32 v24, 1.0, v24
	v_exp_f32_e32 v33, v33
	v_mul_f32_e32 v29, v24, v29
	v_fmamk_f32 v24, v132, 0x3c800000, v4
	v_med3_f32 v24, v24, s57, v196
	v_mul_f32_e32 v30, v30, v31
	v_add_f32_e32 v24, 1.0, v24
	v_add_f32_e32 v31, 1.0, v33
	v_mul_f32_e32 v30, v24, v30
	v_fmamk_f32 v24, v133, 0x3c800000, v5
	v_rcp_f32_e32 v31, v31
	v_med3_f32 v33, v24, s57, v196
	v_mov_b32_e32 v24, v181
	v_cvt_pk_fp8_f32 v24, v23, v25
	v_mov_b32_e32 v25, v181
	v_cvt_pk_fp8_f32 v25, v28, v29
	v_mul_f32_e32 v31, v32, v31
	v_add_f32_e32 v23, 1.0, v33
	v_mul_f32_e32 v23, v23, v31
	v_cvt_pk_fp8_f32 v24, v26, v27 op_sel:[0,0,1]
	v_cvt_pk_fp8_f32 v25, v30, v23 op_sel:[0,0,1]
	v_or_b32_e32 v26, 32, v22
	v_fmamk_f32 v23, v126, 0x3c800000, v14
	v_ashrrev_i32_e32 v27, 31, v26
	v_min_f32_e32 v23, 0x40e00000, v23
	v_lshlrev_b64 v[26:27], 11, v[26:27]
	v_mul_f32_e32 v28, 0xbfd9db23, v23
	v_lshl_add_u64 v[26:27], s[8:9], 0, v[26:27]
	v_mul_f32_e32 v28, 0x3fb8aa3b, v28
	v_exp_f32_e32 v28, v28
	v_lshl_add_u64 v[26:27], v[26:27], 0, v[20:21]
	global_store_dwordx2 v[26:27], v[24:25], off
	v_fmamk_f32 v26, v127, 0x3c800000, v15
	v_min_f32_e32 v26, 0x40e00000, v26
	v_mul_f32_e32 v27, 0xbfd9db23, v26
	v_add_f32_e32 v25, 1.0, v28
	v_mul_f32_e32 v27, 0x3fb8aa3b, v27
	v_rcp_f32_e32 v25, v25
	v_exp_f32_e32 v27, v27
	v_fmamk_f32 v28, v129, 0x3c800000, v17
	v_min_f32_e32 v28, 0x40e00000, v28
	v_mul_f32_e32 v23, v23, v25
	v_add_f32_e32 v25, 1.0, v27
	v_rcp_f32_e32 v25, v25
	v_mul_f32_e32 v29, 0xbfd9db23, v28
	v_mul_f32_e32 v29, 0x3fb8aa3b, v29
	v_exp_f32_e32 v29, v29
	v_mul_f32_e32 v25, v26, v25
	v_fmamk_f32 v26, v128, 0x3c800000, v16
	v_min_f32_e32 v26, 0x40e00000, v26
	v_mul_f32_e32 v27, 0xbfd9db23, v26
;     __device__ __forceinline__ void operator()(const f32x4 (&acc)[2][2][4][2], const Unit& u, int wr, int wc, int fr, int fq) const {
;     ...
;             for (int m = 0; m < 4; ++m) { float r[8];
; #pragma unroll
;                 for (int n = 0; n < 2; ++n)
; #pragma unroll
;                     for (int j = 0; j < 4; ++j) {
;                         float g = acc[ai][0][m][n][j] * W8_INV + bg[n][j], uu = acc[ai][1][m][n][j] * W8_INV + bu[n][j];
;                         g = fminf(g, 7.0f); uu = fminf(fmaxf(uu, -7.0f), 7.0f);
;                         const float glu = g * __builtin_amdgcn_rcpf(1.0f + __expf(-1.702f * g));
;                         r[n * 4 + j] = (uu + 1.0f) * glu; }
;                 u32x2 w; w.x = pk4_fp8(r[0], r[1], r[2], r[3]); w.y = pk4_fp8(r[4], r[5], r[6], r[7]);
;                 *(u32x2*)(O + (size_t)(row0 + ai * HALF + m * 16) * DM + cc) = w; }
; __device__ __forceinline__ SJob sjob_addr(const Args& a, int j, int lane) {
;     SJob c; const int kseg = lane & 7, nq = lane >> 3;
;     if (j < SJOBS_GU) { const int e = j >> 12, kb = (j >> 7) & 31, nb = j & 127, s0 = nb * 32, bj = s0 >> 11, rem = s0 & 2047, pn = rem >> 7, c0 = rem & 127, np = pn * 256 + bj * 128 + c0;
;         c.ld = 4096; c.src = a.w_gate_up + ((size_t)e * 2048 + kb * 64 + kseg * 8) * 4096 + s0 + nq * 4; c.dst = (unsigned char*)(a.ws + WS_WGU_T) + ((size_t)e * 4096 + np + nq * 4) * 2048 + kb * 64 + kseg * 8; }
;     else { const int jj = j - SJOBS_GU, e = jj >> 11, kb = (jj >> 6) & 31, nb = jj & 63;
;         c.ld = 2048; c.src = a.w_down + ((size_t)e * 2048 + kb * 64 + kseg * 8) * 2048 + nb * 32 + nq * 4; c.dst = (unsigned char*)(a.ws + WS_WD_T) + ((size_t)e * 2048 + nb * 32 + nq * 4) * 2048 + kb * 64 + kseg * 8; }
;     return c;
; }
; __device__ __forceinline__ void sjob_load(const SJob& c, f32x4 (&v)[8]) {
; #pragma unroll
;     for (int r = 0; r < 8; ++r) v[r] = __builtin_nontemporal_load((const f32x4*)(c.src + (size_t)r * c.ld));
; }
; __device__ __forceinline__ void sjob_store(const SJob& c, const f32x4 (&v)[8]) {
; #pragma unroll
;     for (int jn = 0; jn < 4; ++jn) { u32x2 o;
;         o.x = pk4_fp8_scaled(v[0][jn], v[1][jn], v[2][jn], v[3][jn]); o.y = pk4_fp8_scaled(v[4][jn], v[5][jn], v[6][jn], v[7][jn]);
;         __builtin_nontemporal_store(o, (u32x2*)(c.dst + (size_t)jn * 2048)); }
; }
	v_mul_f32_e32 v27, 0x3fb8aa3b, v27
	v_exp_f32_e32 v27, v27
	v_fmamk_f32 v30, v119, 0x3c800000, v7
	v_min_f32_e32 v30, 0x40e00000, v30
	v_mul_f32_e32 v31, 0xbfd9db23, v30
	v_add_f32_e32 v27, 1.0, v27
	v_rcp_f32_e32 v27, v27
	v_mul_f32_e32 v31, 0x3fb8aa3b, v31
	v_exp_f32_e32 v31, v31
	v_fmamk_f32 v24, v122, 0x3c800000, v10
	v_mul_f32_e32 v26, v26, v27
	v_add_f32_e32 v27, 1.0, v29
	v_rcp_f32_e32 v27, v27
	v_med3_f32 v24, v24, s57, v196
	v_add_f32_e32 v24, 1.0, v24
	v_mul_f32_e32 v23, v24, v23
	v_mul_f32_e32 v27, v28, v27
	v_fmamk_f32 v28, v118, 0x3c800000, v6
	v_min_f32_e32 v28, 0x40e00000, v28
	v_mul_f32_e32 v29, 0xbfd9db23, v28
	v_mul_f32_e32 v29, 0x3fb8aa3b, v29
	v_exp_f32_e32 v29, v29
	v_fmamk_f32 v24, v123, 0x3c800000, v11
	v_med3_f32 v24, v24, s57, v196
	v_add_f32_e32 v24, 1.0, v24
	v_add_f32_e32 v29, 1.0, v29
	v_rcp_f32_e32 v29, v29
	v_mul_f32_e32 v25, v24, v25
	v_fmamk_f32 v24, v124, 0x3c800000, v12
	v_med3_f32 v24, v24, s57, v196
	v_mul_f32_e32 v28, v28, v29
	v_add_f32_e32 v29, 1.0, v31
	v_rcp_f32_e32 v29, v29
	v_add_f32_e32 v24, 1.0, v24
	v_mul_f32_e32 v26, v24, v26
	v_fmamk_f32 v24, v125, 0x3c800000, v13
	v_mul_f32_e32 v29, v30, v29
	v_fmamk_f32 v30, v120, 0x3c800000, v8
	v_min_f32_e32 v30, 0x40e00000, v30
	v_mul_f32_e32 v31, 0xbfd9db23, v30
	v_med3_f32 v24, v24, s57, v196
	v_mul_f32_e32 v31, 0x3fb8aa3b, v31
	v_add_f32_e32 v24, 1.0, v24
	v_exp_f32_e32 v31, v31
	v_mul_f32_e32 v27, v24, v27
	v_fmamk_f32 v24, v114, 0x3c800000, v2
	v_med3_f32 v24, v24, s57, v196
	v_fmamk_f32 v32, v121, 0x3c800000, v9
	v_add_f32_e32 v24, 1.0, v24
	v_min_f32_e32 v32, 0x40e00000, v32
	v_mul_f32_e32 v28, v24, v28
	v_fmamk_f32 v24, v115, 0x3c800000, v3
	v_add_f32_e32 v31, 1.0, v31
	v_mul_f32_e32 v33, 0xbfd9db23, v32
	v_med3_f32 v24, v24, s57, v196
	v_rcp_f32_e32 v31, v31
	v_mul_f32_e32 v33, 0x3fb8aa3b, v33
	v_add_f32_e32 v24, 1.0, v24
	v_exp_f32_e32 v33, v33
	v_mul_f32_e32 v29, v24, v29
	v_fmamk_f32 v24, v116, 0x3c800000, v4
	v_med3_f32 v24, v24, s57, v196
	v_mul_f32_e32 v30, v30, v31
	v_add_f32_e32 v24, 1.0, v24
	v_add_f32_e32 v31, 1.0, v33
	v_mul_f32_e32 v30, v24, v30
	v_fmamk_f32 v24, v117, 0x3c800000, v5
	v_rcp_f32_e32 v31, v31
	v_med3_f32 v33, v24, s57, v196
	v_mov_b32_e32 v24, v181
	v_cvt_pk_fp8_f32 v24, v23, v25
	v_mov_b32_e32 v25, v181
	v_cvt_pk_fp8_f32 v25, v28, v29
	v_mul_f32_e32 v31, v32, v31
	v_add_f32_e32 v23, 1.0, v33
	v_mul_f32_e32 v23, v23, v31
	v_or_b32_e32 v22, 48, v22
	v_cvt_pk_fp8_f32 v25, v30, v23 op_sel:[0,0,1]
	v_ashrrev_i32_e32 v23, 31, v22
	v_lshlrev_b64 v[22:23], 11, v[22:23]
	v_lshl_add_u64 v[22:23], s[8:9], 0, v[22:23]
	v_lshl_add_u64 v[20:21], v[22:23], 0, v[20:21]
	v_fmamk_f32 v22, v111, 0x3c800000, v15
	v_min_f32_e32 v22, 0x40e00000, v22
	v_mul_f32_e32 v23, 0xbfd9db23, v22
	v_mul_f32_e32 v23, 0x3fb8aa3b, v23
	v_exp_f32_e32 v23, v23
	v_cvt_pk_fp8_f32 v24, v26, v27 op_sel:[0,0,1]
	v_fmamk_f32 v26, v110, 0x3c800000, v14
	v_min_f32_e32 v26, 0x40e00000, v26
	v_add_f32_e32 v23, 1.0, v23
	v_mul_f32_e32 v27, 0xbfd9db23, v26
	v_rcp_f32_e32 v23, v23
	v_mul_f32_e32 v27, 0x3fb8aa3b, v27
	v_exp_f32_e32 v27, v27
	global_store_dwordx2 v[20:21], v[24:25], off
	s_cmp_lg_u32 s82, 0
	s_cbranch_scc0 .Lesj_mid_skip
	s_waitcnt vmcnt(4)
	v_cvt_scalef32_pk_fp8_f32 v250, v218, v222, v254
	v_cvt_scalef32_pk_fp8_f32 v251, v234, v238, v254
	v_cvt_scalef32_pk_fp8_f32 v250, v226, v230, v254 op_sel:[0,0,0,1]
	v_cvt_scalef32_pk_fp8_f32 v251, v242, v246, v254 op_sel:[0,0,0,1]
	global_store_dwordx2 v253, v[250:251], s[90:91] nt
	v_cvt_scalef32_pk_fp8_f32 v250, v219, v223, v254
	v_cvt_scalef32_pk_fp8_f32 v251, v235, v239, v254
	v_cvt_scalef32_pk_fp8_f32 v250, v227, v231, v254 op_sel:[0,0,0,1]
	v_cvt_scalef32_pk_fp8_f32 v251, v243, v247, v254 op_sel:[0,0,0,1]
	global_store_dwordx2 v253, v[250:251], s[90:91] offset:2048 nt
	v_cvt_scalef32_pk_fp8_f32 v250, v220, v224, v254
	v_cvt_scalef32_pk_fp8_f32 v251, v236, v240, v254
	v_cvt_scalef32_pk_fp8_f32 v250, v228, v232, v254 op_sel:[0,0,0,1]
	v_cvt_scalef32_pk_fp8_f32 v251, v244, v248, v254 op_sel:[0,0,0,1]
	s_add_u32 s90, s90, 0x1000
	s_addc_u32 s91, s91, 0
	global_store_dwordx2 v253, v[250:251], s[90:91] nt
	v_cvt_scalef32_pk_fp8_f32 v250, v221, v225, v254
	v_cvt_scalef32_pk_fp8_f32 v251, v237, v241, v254
	v_cvt_scalef32_pk_fp8_f32 v250, v229, v233, v254 op_sel:[0,0,0,1]
	v_cvt_scalef32_pk_fp8_f32 v251, v245, v249, v254 op_sel:[0,0,0,1]
	global_store_dwordx2 v253, v[250:251], s[90:91] offset:2048 nt
	s_add_i32 s98, s98, 1
	s_lshr_b32 s90, s98, 1
	s_mul_i32 s90, s90, s83
	s_add_i32 s90, s90, s84
	s_cmp_lt_u32 s90, 0x8000
	s_cbranch_scc0 .Lesj_mid_no
	s_lshr_b32 s91, s90, 10
	s_lshl_b32 s91, s91, 11
	s_and_b32 s99, s90, 0x3c0
	s_lshl_b32 s99, s99, 1
	s_or_b32 s91, s91, s99
	s_and_b32 s99, s98, 1
	s_lshl_b32 s99, s99, 6
	s_or_b32 s91, s91, s99
	s_and_b32 s90, s90, 63
	s_or_b32 s90, s90, s91
	s_lshr_b32 s91, s90, 11
	s_and_b32 s99, s90, 0x7c0
	s_and_b32 s82, s90, 63
	s_lshl_b32 s32, s91, 24
	s_lshl_b32 s100, s99, 13
	s_add_i32 s32, s32, s100
	s_lshl_b32 s100, s82, 7
	s_add_i32 s32, s32, s100
	s_add_u32 s100, s86, s32
	s_addc_u32 s101, s87, 0
	s_lshl_b32 s32, s91, 22
	s_lshl_b32 s82, s82, 16
	s_add_i32 s32, s32, s82
	s_add_i32 s32, s32, s99
	s_add_u32 s90, s88, s32
	s_addc_u32 s91, s89, 0
	global_load_dwordx4 v[218:221], v252, s[100:101] nt
	s_add_u32 s100, s100, 0x2000
	s_addc_u32 s101, s101, 0
	global_load_dwordx4 v[222:225], v252, s[100:101] nt
	s_add_u32 s100, s100, 0x2000
	s_addc_u32 s101, s101, 0
	global_load_dwordx4 v[226:229], v252, s[100:101] nt
	s_add_u32 s100, s100, 0x2000
	s_addc_u32 s101, s101, 0
	global_load_dwordx4 v[230:233], v252, s[100:101] nt
	s_add_u32 s100, s100, 0x2000
	s_addc_u32 s101, s101, 0
	global_load_dwordx4 v[234:237], v252, s[100:101] nt
	s_add_u32 s100, s100, 0x2000
	s_addc_u32 s101, s101, 0
	global_load_dwordx4 v[238:241], v252, s[100:101] nt
	s_add_u32 s100, s100, 0x2000
	s_addc_u32 s101, s101, 0
	global_load_dwordx4 v[242:245], v252, s[100:101] nt
	s_add_u32 s100, s100, 0x2000
	s_addc_u32 s101, s101, 0
	global_load_dwordx4 v[246:249], v252, s[100:101] nt
	s_mov_b32 s82, 1
	s_branch .Lesj_mid_skip

; __device__ __forceinline__ unsigned pk4_fp8(float a, float b, float c, float d) { int p = __builtin_amdgcn_cvt_pk_fp8_f32(a, b, 0, false); p = __builtin_amdgcn_cvt_pk_fp8_f32(c, d, p, true); return (unsigned)p; }
;     __device__ __forceinline__ void operator()(const f32x4 (&acc)[2][2][4][2], const Unit& u, int wr, int wc, int fr, int fq) const {
;     ...
;             for (int m = 0; m < 4; ++m) { float r[8];
; #pragma unroll
;                 for (int n = 0; n < 2; ++n)
; #pragma unroll
;                     for (int j = 0; j < 4; ++j) {
;                         float g = acc[ai][0][m][n][j] * W8_INV + bg[n][j], uu = acc[ai][1][m][n][j] * W8_INV + bu[n][j];
;                         g = fminf(g, 7.0f); uu = fminf(fmaxf(uu, -7.0f), 7.0f);
;                         const float glu = g * __builtin_amdgcn_rcpf(1.0f + __expf(-1.702f * g));
;                         r[n * 4 + j] = (uu + 1.0f) * glu; }
;                 u32x2 w; w.x = pk4_fp8(r[0], r[1], r[2], r[3]); w.y = pk4_fp8(r[4], r[5], r[6], r[7]);
;                 *(u32x2*)(O + (size_t)(row0 + ai * HALF + m * 16) * DM + cc) = w; }
.Lesj_mid_skip:
	v_mul_f32_e32 v22, v22, v23
	v_fmamk_f32 v23, v112, 0x3c800000, v16
	v_min_f32_e32 v23, 0x40e00000, v23
	v_add_f32_e32 v21, 1.0, v27
	v_mul_f32_e32 v24, 0xbfd9db23, v23
	v_rcp_f32_e32 v21, v21
	v_mul_f32_e32 v24, 0x3fb8aa3b, v24
	v_exp_f32_e32 v24, v24
	v_fmamk_f32 v25, v113, 0x3c800000, v17
	v_min_f32_e32 v25, 0x40e00000, v25
	v_mul_f32_e32 v21, v26, v21
	v_mul_f32_e32 v26, 0xbfd9db23, v25
	v_add_f32_e32 v24, 1.0, v24
	v_mul_f32_e32 v26, 0x3fb8aa3b, v26
	v_rcp_f32_e32 v24, v24
	v_exp_f32_e32 v26, v26
	v_fmamk_f32 v27, v103, 0x3c800000, v7
	v_min_f32_e32 v27, 0x40e00000, v27
	v_mul_f32_e32 v23, v23, v24
	v_add_f32_e32 v24, 1.0, v26
	v_rcp_f32_e32 v24, v24
	v_mul_f32_e32 v28, 0xbfd9db23, v27
	v_mul_f32_e32 v28, 0x3fb8aa3b, v28
	v_exp_f32_e32 v28, v28
	v_mul_f32_e32 v24, v25, v24
	v_fmamk_f32 v25, v102, 0x3c800000, v6
	v_min_f32_e32 v25, 0x40e00000, v25
	v_mul_f32_e32 v26, 0xbfd9db23, v25
	v_mul_f32_e32 v26, 0x3fb8aa3b, v26
	v_exp_f32_e32 v26, v26
	v_fmamk_f32 v20, v106, 0x3c800000, v10
	v_med3_f32 v20, v20, s57, v196
	v_add_f32_e32 v20, 1.0, v20
	v_add_f32_e32 v26, 1.0, v26
	v_rcp_f32_e32 v26, v26
	v_mul_f32_e32 v21, v20, v21
	v_fmamk_f32 v20, v107, 0x3c800000, v11
	v_med3_f32 v20, v20, s57, v196
	v_mul_f32_e32 v25, v25, v26
	v_add_f32_e32 v26, 1.0, v28
	v_rcp_f32_e32 v26, v26
	v_add_f32_e32 v20, 1.0, v20
	v_mul_f32_e32 v22, v20, v22
	v_fmamk_f32 v20, v108, 0x3c800000, v12
	v_med3_f32 v20, v20, s57, v196
	v_mul_f32_e32 v26, v27, v26
	v_fmamk_f32 v27, v104, 0x3c800000, v8
	v_add_f32_e32 v20, 1.0, v20
	v_min_f32_e32 v27, 0x40e00000, v27
	v_mul_f32_e32 v23, v20, v23
	v_fmamk_f32 v20, v109, 0x3c800000, v13
	v_mul_f32_e32 v28, 0xbfd9db23, v27
	v_med3_f32 v20, v20, s57, v196
	v_mul_f32_e32 v28, 0x3fb8aa3b, v28
	v_add_f32_e32 v20, 1.0, v20
	v_exp_f32_e32 v28, v28
	v_mul_f32_e32 v24, v20, v24
	v_fmamk_f32 v20, v98, 0x3c800000, v2
	v_med3_f32 v20, v20, s57, v196
	v_fmamk_f32 v29, v105, 0x3c800000, v9
	v_add_f32_e32 v20, 1.0, v20
	v_min_f32_e32 v29, 0x40e00000, v29
	v_mul_f32_e32 v25, v20, v25
	v_fmamk_f32 v20, v99, 0x3c800000, v3
	v_add_f32_e32 v28, 1.0, v28
	v_mul_f32_e32 v30, 0xbfd9db23, v29
	v_med3_f32 v20, v20, s57, v196
	v_rcp_f32_e32 v28, v28
	v_mul_f32_e32 v30, 0x3fb8aa3b, v30
	v_add_f32_e32 v20, 1.0, v20
	v_exp_f32_e32 v30, v30
	v_mul_f32_e32 v26, v20, v26
	v_fmamk_f32 v20, v100, 0x3c800000, v4
	v_med3_f32 v20, v20, s57, v196
	v_mul_f32_e32 v27, v27, v28
	v_add_f32_e32 v20, 1.0, v20
	v_add_f32_e32 v28, 1.0, v30
	v_mul_f32_e32 v27, v20, v27
	v_fmamk_f32 v20, v101, 0x3c800000, v5
	v_rcp_f32_e32 v28, v28
	v_med3_f32 v30, v20, s57, v196
	v_mov_b32_e32 v20, v181
	v_cvt_pk_fp8_f32 v20, v21, v22
	v_mov_b32_e32 v21, v181
	v_cvt_pk_fp8_f32 v21, v25, v26
	v_mul_f32_e32 v28, v29, v28
	v_add_f32_e32 v22, 1.0, v30
	v_mul_f32_e32 v22, v22, v28
	v_cvt_pk_fp8_f32 v21, v27, v22 op_sel:[0,0,1]
	v_fmamk_f32 v22, v94, 0x3c800000, v14
	v_cvt_pk_fp8_f32 v20, v23, v24 op_sel:[0,0,1]
	v_min_f32_e32 v24, 0x40e00000, v22
	v_mul_f32_e32 v22, 0xbfd9db23, v24
	v_mul_f32_e32 v22, 0x3fb8aa3b, v22
	v_exp_f32_e32 v25, v22
	v_add_co_u32_e32 v22, vcc, s58, v18
	v_fmamk_f32 v27, v87, 0x3c800000, v7
	s_nop 0
	v_addc_co_u32_e32 v23, vcc, 0, v19, vcc
	global_store_dwordx2 v[22:23], v[20:21], off
	v_fmamk_f32 v22, v95, 0x3c800000, v15
	v_min_f32_e32 v22, 0x40e00000, v22
	v_mul_f32_e32 v23, 0xbfd9db23, v22
	v_mul_f32_e32 v23, 0x3fb8aa3b, v23
	v_exp_f32_e32 v23, v23
	v_add_f32_e32 v21, 1.0, v25
	v_rcp_f32_e32 v21, v21
	v_fmamk_f32 v25, v97, 0x3c800000, v17
	v_add_f32_e32 v23, 1.0, v23
	v_rcp_f32_e32 v23, v23
	v_mul_f32_e32 v21, v24, v21
	v_min_f32_e32 v25, 0x40e00000, v25
	v_mul_f32_e32 v26, 0xbfd9db23, v25
	v_mul_f32_e32 v22, v22, v23
	v_fmamk_f32 v23, v96, 0x3c800000, v16
	v_min_f32_e32 v23, 0x40e00000, v23
	v_mul_f32_e32 v24, 0xbfd9db23, v23
	v_mul_f32_e32 v24, 0x3fb8aa3b, v24
	v_exp_f32_e32 v24, v24
	v_mul_f32_e32 v26, 0x3fb8aa3b, v26
	v_exp_f32_e32 v26, v26
	v_min_f32_e32 v27, 0x40e00000, v27
	v_add_f32_e32 v24, 1.0, v24
	v_rcp_f32_e32 v24, v24
	v_mul_f32_e32 v28, 0xbfd9db23, v27
	v_mul_f32_e32 v28, 0x3fb8aa3b, v28
	v_exp_f32_e32 v28, v28
	v_mul_f32_e32 v23, v23, v24
	v_add_f32_e32 v24, 1.0, v26
	v_rcp_f32_e32 v24, v24
	v_fmamk_f32 v20, v90, 0x3c800000, v10
	v_med3_f32 v20, v20, s57, v196
	v_add_f32_e32 v20, 1.0, v20
	v_mul_f32_e32 v24, v25, v24
	v_fmamk_f32 v25, v86, 0x3c800000, v6
	v_min_f32_e32 v25, 0x40e00000, v25
	v_mul_f32_e32 v26, 0xbfd9db23, v25
	v_mul_f32_e32 v26, 0x3fb8aa3b, v26
	v_exp_f32_e32 v26, v26
	v_mul_f32_e32 v21, v20, v21
	v_fmamk_f32 v20, v91, 0x3c800000, v11
	v_med3_f32 v20, v20, s57, v196
	v_add_f32_e32 v26, 1.0, v26
	v_rcp_f32_e32 v26, v26
	v_add_f32_e32 v20, 1.0, v20
	v_mul_f32_e32 v22, v20, v22
	v_fmamk_f32 v20, v92, 0x3c800000, v12
	v_mul_f32_e32 v25, v25, v26
	v_add_f32_e32 v26, 1.0, v28
	v_rcp_f32_e32 v26, v26
	v_med3_f32 v20, v20, s57, v196
	v_add_f32_e32 v20, 1.0, v20
	v_mul_f32_e32 v23, v20, v23
	v_mul_f32_e32 v26, v27, v26
	v_fmamk_f32 v27, v88, 0x3c800000, v8
	v_min_f32_e32 v27, 0x40e00000, v27
	v_fmamk_f32 v20, v93, 0x3c800000, v13
	v_mul_f32_e32 v28, 0xbfd9db23, v27
	v_med3_f32 v20, v20, s57, v196
	v_mul_f32_e32 v28, 0x3fb8aa3b, v28
	v_add_f32_e32 v20, 1.0, v20
	v_exp_f32_e32 v28, v28
	v_mul_f32_e32 v24, v20, v24
	v_fmamk_f32 v20, v82, 0x3c800000, v2
	v_med3_f32 v20, v20, s57, v196
	v_fmamk_f32 v29, v89, 0x3c800000, v9
	v_add_f32_e32 v20, 1.0, v20
	v_min_f32_e32 v29, 0x40e00000, v29
	v_mul_f32_e32 v25, v20, v25
	v_fmamk_f32 v20, v83, 0x3c800000, v3
	v_add_f32_e32 v28, 1.0, v28
	v_mul_f32_e32 v30, 0xbfd9db23, v29
	v_med3_f32 v20, v20, s57, v196
	v_rcp_f32_e32 v28, v28
	v_mul_f32_e32 v30, 0x3fb8aa3b, v30
	v_add_f32_e32 v20, 1.0, v20
; __device__ __forceinline__ unsigned pk4_fp8(float a, float b, float c, float d) { int p = __builtin_amdgcn_cvt_pk_fp8_f32(a, b, 0, false); p = __builtin_amdgcn_cvt_pk_fp8_f32(c, d, p, true); return (unsigned)p; }
;     __device__ __forceinline__ void operator()(const f32x4 (&acc)[2][2][4][2], const Unit& u, int wr, int wc, int fr, int fq) const {
;     ...
;             for (int m = 0; m < 4; ++m) { float r[8];
; #pragma unroll
;                 for (int n = 0; n < 2; ++n)
; #pragma unroll
;                     for (int j = 0; j < 4; ++j) {
;                         float g = acc[ai][0][m][n][j] * W8_INV + bg[n][j], uu = acc[ai][1][m][n][j] * W8_INV + bu[n][j];
;                         g = fminf(g, 7.0f); uu = fminf(fmaxf(uu, -7.0f), 7.0f);
;                         const float glu = g * __builtin_amdgcn_rcpf(1.0f + __expf(-1.702f * g));
;                         r[n * 4 + j] = (uu + 1.0f) * glu; }
;                 u32x2 w; w.x = pk4_fp8(r[0], r[1], r[2], r[3]); w.y = pk4_fp8(r[4], r[5], r[6], r[7]);
;                 *(u32x2*)(O + (size_t)(row0 + ai * HALF + m * 16) * DM + cc) = w; }
	v_exp_f32_e32 v30, v30
	v_mul_f32_e32 v26, v20, v26
	v_fmamk_f32 v20, v84, 0x3c800000, v4
	v_med3_f32 v20, v20, s57, v196
	v_mul_f32_e32 v27, v27, v28
	v_add_f32_e32 v20, 1.0, v20
	v_add_f32_e32 v28, 1.0, v30
	v_mul_f32_e32 v27, v20, v27
	v_fmamk_f32 v20, v85, 0x3c800000, v5
	v_rcp_f32_e32 v28, v28
	v_med3_f32 v30, v20, s57, v196
	v_mov_b32_e32 v20, v181
	v_cvt_pk_fp8_f32 v20, v21, v22
	v_mov_b32_e32 v21, v181
	v_cvt_pk_fp8_f32 v21, v25, v26
	v_mul_f32_e32 v28, v29, v28
	v_add_f32_e32 v22, 1.0, v30
	v_mul_f32_e32 v22, v22, v28
	v_cvt_pk_fp8_f32 v21, v27, v22 op_sel:[0,0,1]
	v_fmamk_f32 v22, v78, 0x3c800000, v14
	v_cvt_pk_fp8_f32 v20, v23, v24 op_sel:[0,0,1]
	v_min_f32_e32 v24, 0x40e00000, v22
	v_mul_f32_e32 v22, 0xbfd9db23, v24
	v_mul_f32_e32 v22, 0x3fb8aa3b, v22
	v_exp_f32_e32 v25, v22
	v_add_co_u32_e32 v22, vcc, s59, v18
	v_fmamk_f32 v27, v71, 0x3c800000, v7
	s_nop 0
	v_addc_co_u32_e32 v23, vcc, 0, v19, vcc
	global_store_dwordx2 v[22:23], v[20:21], off
	v_fmamk_f32 v22, v79, 0x3c800000, v15
	v_min_f32_e32 v22, 0x40e00000, v22
	v_mul_f32_e32 v23, 0xbfd9db23, v22
	v_mul_f32_e32 v23, 0x3fb8aa3b, v23
	v_exp_f32_e32 v23, v23
	v_add_f32_e32 v21, 1.0, v25
	v_rcp_f32_e32 v21, v21
	v_fmamk_f32 v25, v81, 0x3c800000, v17
	v_add_f32_e32 v23, 1.0, v23
	v_rcp_f32_e32 v23, v23
	v_mul_f32_e32 v21, v24, v21
	v_min_f32_e32 v25, 0x40e00000, v25
	v_mul_f32_e32 v26, 0xbfd9db23, v25
	v_mul_f32_e32 v22, v22, v23
	v_fmamk_f32 v23, v80, 0x3c800000, v16
	v_min_f32_e32 v23, 0x40e00000, v23
	v_mul_f32_e32 v24, 0xbfd9db23, v23
	v_mul_f32_e32 v24, 0x3fb8aa3b, v24
	v_exp_f32_e32 v24, v24
	v_mul_f32_e32 v26, 0x3fb8aa3b, v26
	v_exp_f32_e32 v26, v26
	v_min_f32_e32 v27, 0x40e00000, v27
	v_add_f32_e32 v24, 1.0, v24
	v_rcp_f32_e32 v24, v24
	v_mul_f32_e32 v28, 0xbfd9db23, v27
	v_mul_f32_e32 v28, 0x3fb8aa3b, v28
	v_exp_f32_e32 v28, v28
	v_mul_f32_e32 v23, v23, v24
	v_add_f32_e32 v24, 1.0, v26
	v_rcp_f32_e32 v24, v24
	v_fmamk_f32 v20, v74, 0x3c800000, v10
	v_med3_f32 v20, v20, s57, v196
	v_add_f32_e32 v20, 1.0, v20
	v_mul_f32_e32 v24, v25, v24
	v_fmamk_f32 v25, v70, 0x3c800000, v6
	v_min_f32_e32 v25, 0x40e00000, v25
	v_mul_f32_e32 v26, 0xbfd9db23, v25
	v_mul_f32_e32 v26, 0x3fb8aa3b, v26
	v_exp_f32_e32 v26, v26
	v_mul_f32_e32 v21, v20, v21
	v_fmamk_f32 v20, v75, 0x3c800000, v11
	v_med3_f32 v20, v20, s57, v196
	v_add_f32_e32 v26, 1.0, v26
	v_rcp_f32_e32 v26, v26
	v_add_f32_e32 v20, 1.0, v20
	v_mul_f32_e32 v22, v20, v22
	v_fmamk_f32 v20, v76, 0x3c800000, v12
	v_mul_f32_e32 v25, v25, v26
	v_add_f32_e32 v26, 1.0, v28
	v_rcp_f32_e32 v26, v26
	v_med3_f32 v20, v20, s57, v196
	v_add_f32_e32 v20, 1.0, v20
	v_mul_f32_e32 v23, v20, v23
	v_mul_f32_e32 v26, v27, v26
	v_fmamk_f32 v27, v72, 0x3c800000, v8
	v_min_f32_e32 v27, 0x40e00000, v27
	v_fmamk_f32 v20, v77, 0x3c800000, v13
	v_mul_f32_e32 v28, 0xbfd9db23, v27
	v_med3_f32 v20, v20, s57, v196
	v_mul_f32_e32 v28, 0x3fb8aa3b, v28
	v_add_f32_e32 v20, 1.0, v20
	v_exp_f32_e32 v28, v28
	v_mul_f32_e32 v24, v20, v24
	v_fmamk_f32 v20, v66, 0x3c800000, v2
	v_med3_f32 v20, v20, s57, v196
	v_fmamk_f32 v29, v73, 0x3c800000, v9
	v_add_f32_e32 v20, 1.0, v20
	v_min_f32_e32 v29, 0x40e00000, v29
	v_mul_f32_e32 v25, v20, v25
	v_fmamk_f32 v20, v67, 0x3c800000, v3
	v_add_f32_e32 v28, 1.0, v28
	v_mul_f32_e32 v30, 0xbfd9db23, v29
	v_med3_f32 v20, v20, s57, v196
	v_rcp_f32_e32 v28, v28
	v_mul_f32_e32 v30, 0x3fb8aa3b, v30
	v_add_f32_e32 v20, 1.0, v20
	v_exp_f32_e32 v30, v30
	v_mul_f32_e32 v26, v20, v26
	v_fmamk_f32 v20, v68, 0x3c800000, v4
	v_med3_f32 v20, v20, s57, v196
	v_mul_f32_e32 v27, v27, v28
	v_add_f32_e32 v20, 1.0, v20
	v_add_f32_e32 v28, 1.0, v30
	v_mul_f32_e32 v27, v20, v27
	v_fmamk_f32 v20, v69, 0x3c800000, v5
	v_rcp_f32_e32 v28, v28
	v_med3_f32 v30, v20, s57, v196
	v_mov_b32_e32 v20, v181
	v_cvt_pk_fp8_f32 v20, v21, v22
	v_mov_b32_e32 v21, v181
	v_cvt_pk_fp8_f32 v21, v25, v26
	v_mul_f32_e32 v28, v29, v28
	v_add_f32_e32 v22, 1.0, v30
	v_fmamk_f32 v14, v62, 0x3c800000, v14
	v_mul_f32_e32 v22, v22, v28
	v_min_f32_e32 v14, 0x40e00000, v14
	v_cvt_pk_fp8_f32 v21, v27, v22 op_sel:[0,0,1]
	v_mul_f32_e32 v22, 0xbfd9db23, v14
	v_cvt_pk_fp8_f32 v20, v23, v24 op_sel:[0,0,1]
	v_mul_f32_e32 v22, 0x3fb8aa3b, v22
	v_exp_f32_e32 v24, v22
	v_add_co_u32_e32 v22, vcc, s60, v18
	v_fmamk_f32 v15, v63, 0x3c800000, v15
	s_nop 0
	v_addc_co_u32_e32 v23, vcc, 0, v19, vcc
	v_min_f32_e32 v15, 0x40e00000, v15
	global_store_dwordx2 v[22:23], v[20:21], off
; __device__ __forceinline__ unsigned pk4_fp8(float a, float b, float c, float d) { int p = __builtin_amdgcn_cvt_pk_fp8_f32(a, b, 0, false); p = __builtin_amdgcn_cvt_pk_fp8_f32(c, d, p, true); return (unsigned)p; }
; __device__ __forceinline__ unsigned pk4_fp8_scaled(float a, float b, float c, float d) { s16x2 r = {0, 0}; r = __builtin_amdgcn_cvt_scalef32_pk_fp8_f32(r, a, b, pg8::W8_INV, false); r = __builtin_amdgcn_cvt_scalef32_pk_fp8_f32(r, c, d, pg8::W8_INV, true); return __builtin_bit_cast(unsigned, r); }
;     __device__ __forceinline__ void operator()(const f32x4 (&acc)[2][2][4][2], const Unit& u, int wr, int wc, int fr, int fq) const {
;     ...
;             for (int m = 0; m < 4; ++m) { float r[8];
; #pragma unroll
;                 for (int n = 0; n < 2; ++n)
; #pragma unroll
;                     for (int j = 0; j < 4; ++j) {
;                         float g = acc[ai][0][m][n][j] * W8_INV + bg[n][j], uu = acc[ai][1][m][n][j] * W8_INV + bu[n][j];
;                         g = fminf(g, 7.0f); uu = fminf(fmaxf(uu, -7.0f), 7.0f);
;                         const float glu = g * __builtin_amdgcn_rcpf(1.0f + __expf(-1.702f * g));
;                         r[n * 4 + j] = (uu + 1.0f) * glu; }
;                 u32x2 w; w.x = pk4_fp8(r[0], r[1], r[2], r[3]); w.y = pk4_fp8(r[4], r[5], r[6], r[7]);
;                 *(u32x2*)(O + (size_t)(row0 + ai * HALF + m * 16) * DM + cc) = w; }
; __device__ __forceinline__ void sjob_store(const SJob& c, const f32x4 (&v)[8]) {
; #pragma unroll
;     for (int jn = 0; jn < 4; ++jn) { u32x2 o;
;         o.x = pk4_fp8_scaled(v[0][jn], v[1][jn], v[2][jn], v[3][jn]); o.y = pk4_fp8_scaled(v[4][jn], v[5][jn], v[6][jn], v[7][jn]);
;         __builtin_nontemporal_store(o, (u32x2*)(c.dst + (size_t)jn * 2048)); }
; }
	v_mul_f32_e32 v21, 0xbfd9db23, v15
	v_add_f32_e32 v20, 1.0, v24
	v_mul_f32_e32 v21, 0x3fb8aa3b, v21
	v_rcp_f32_e32 v20, v20
	v_exp_f32_e32 v21, v21
	v_fmamk_f32 v10, v58, 0x3c800000, v10
	v_med3_f32 v10, v10, s57, v196
	v_mul_f32_e32 v14, v14, v20
	v_add_f32_e32 v20, 1.0, v21
	v_rcp_f32_e32 v20, v20
	v_add_f32_e32 v10, 1.0, v10
	v_mul_f32_e32 v10, v10, v14
	v_fmamk_f32 v11, v59, 0x3c800000, v11
	v_mul_f32_e32 v14, v15, v20
	v_fmamk_f32 v15, v64, 0x3c800000, v16
	v_min_f32_e32 v15, 0x40e00000, v15
	v_mul_f32_e32 v16, 0xbfd9db23, v15
	v_mul_f32_e32 v16, 0x3fb8aa3b, v16
	v_exp_f32_e32 v16, v16
	v_med3_f32 v11, v11, s57, v196
	v_add_f32_e32 v11, 1.0, v11
	v_fmac_f32_e32 v17, 0x3c800000, v65
	v_mul_f32_e32 v11, v11, v14
	v_add_f32_e32 v14, 1.0, v16
	v_min_f32_e32 v16, 0x40e00000, v17
	v_mul_f32_e32 v17, 0xbfd9db23, v16
	v_mul_f32_e32 v17, 0x3fb8aa3b, v17
	v_rcp_f32_e32 v14, v14
	v_exp_f32_e32 v17, v17
	v_fmamk_f32 v12, v60, 0x3c800000, v12
	v_med3_f32 v12, v12, s57, v196
	v_mul_f32_e32 v14, v15, v14
	v_add_f32_e32 v15, 1.0, v17
	v_rcp_f32_e32 v15, v15
	v_fmamk_f32 v6, v54, 0x3c800000, v6
	v_add_f32_e32 v12, 1.0, v12
	v_min_f32_e32 v6, 0x40e00000, v6
	v_mul_f32_e32 v12, v12, v14
	v_mul_f32_e32 v14, v16, v15
	v_mul_f32_e32 v15, 0xbfd9db23, v6
	v_mul_f32_e32 v15, 0x3fb8aa3b, v15
	v_exp_f32_e32 v15, v15
	v_fmac_f32_e32 v13, 0x3c800000, v61
	v_med3_f32 v13, v13, s57, v196
	v_fmamk_f32 v7, v55, 0x3c800000, v7
	v_add_f32_e32 v13, 1.0, v13
	v_min_f32_e32 v7, 0x40e00000, v7
	v_mul_f32_e32 v13, v13, v14
	v_add_f32_e32 v14, 1.0, v15
	v_mul_f32_e32 v15, 0xbfd9db23, v7
	v_mul_f32_e32 v15, 0x3fb8aa3b, v15
	v_rcp_f32_e32 v14, v14
	v_exp_f32_e32 v15, v15
	v_fmamk_f32 v2, v50, 0x3c800000, v2
	v_med3_f32 v2, v2, s57, v196
	v_mul_f32_e32 v6, v6, v14
	v_add_f32_e32 v14, 1.0, v15
	v_rcp_f32_e32 v14, v14
	v_add_f32_e32 v2, 1.0, v2
	v_mul_f32_e32 v6, v2, v6
	v_fmamk_f32 v2, v51, 0x3c800000, v3
	v_mul_f32_e32 v3, v7, v14
	v_fmamk_f32 v7, v56, 0x3c800000, v8
	v_min_f32_e32 v7, 0x40e00000, v7
	v_mul_f32_e32 v8, 0xbfd9db23, v7
	v_mul_f32_e32 v8, 0x3fb8aa3b, v8
	v_exp_f32_e32 v8, v8
	v_med3_f32 v2, v2, s57, v196
	v_add_f32_e32 v2, 1.0, v2
	v_fmac_f32_e32 v9, 0x3c800000, v57
	v_mul_f32_e32 v14, v2, v3
	v_fmamk_f32 v2, v52, 0x3c800000, v4
	v_min_f32_e32 v4, 0x40e00000, v9
	v_add_f32_e32 v3, 1.0, v8
	v_mul_f32_e32 v8, 0xbfd9db23, v4
	v_mul_f32_e32 v8, 0x3fb8aa3b, v8
	v_rcp_f32_e32 v3, v3
	v_exp_f32_e32 v8, v8
	v_med3_f32 v2, v2, s57, v196
	v_add_f32_e32 v2, 1.0, v2
	v_mul_f32_e32 v3, v7, v3
	v_add_f32_e32 v7, 1.0, v8
	v_rcp_f32_e32 v7, v7
	v_mul_f32_e32 v8, v2, v3
	v_mov_b32_e32 v2, v181
	v_mov_b32_e32 v3, v181
	v_fmac_f32_e32 v5, 0x3c800000, v53
	v_cvt_pk_fp8_f32 v2, v10, v11
	v_cvt_pk_fp8_f32 v3, v6, v14
	v_med3_f32 v5, v5, s57, v196
	v_mul_f32_e32 v4, v4, v7
	v_add_f32_e32 v5, 1.0, v5
	v_mul_f32_e32 v4, v5, v4
	v_cvt_pk_fp8_f32 v2, v12, v13 op_sel:[0,0,1]
	v_cvt_pk_fp8_f32 v3, v8, v4 op_sel:[0,0,1]
	v_add_co_u32_e32 v4, vcc, 0x58000, v18
	s_nop 1
	v_addc_co_u32_e32 v5, vcc, 0, v19, vcc
	s_and_b64 vcc, exec, s[22:23]
	global_store_dwordx2 v[4:5], v[2:3], off
	s_cmp_lg_u32 s82, 0
	s_cbranch_scc0 .Lesj_skip
	s_waitcnt vmcnt(4)
	v_cvt_scalef32_pk_fp8_f32 v250, v218, v222, v254
	v_cvt_scalef32_pk_fp8_f32 v251, v234, v238, v254
	v_cvt_scalef32_pk_fp8_f32 v250, v226, v230, v254 op_sel:[0,0,0,1]
	v_cvt_scalef32_pk_fp8_f32 v251, v242, v246, v254 op_sel:[0,0,0,1]
	global_store_dwordx2 v253, v[250:251], s[90:91] nt
	v_cvt_scalef32_pk_fp8_f32 v250, v219, v223, v254
	v_cvt_scalef32_pk_fp8_f32 v251, v235, v239, v254
	v_cvt_scalef32_pk_fp8_f32 v250, v227, v231, v254 op_sel:[0,0,0,1]
	v_cvt_scalef32_pk_fp8_f32 v251, v243, v247, v254 op_sel:[0,0,0,1]
	global_store_dwordx2 v253, v[250:251], s[90:91] offset:2048 nt
	v_cvt_scalef32_pk_fp8_f32 v250, v220, v224, v254
	v_cvt_scalef32_pk_fp8_f32 v251, v236, v240, v254
	v_cvt_scalef32_pk_fp8_f32 v250, v228, v232, v254 op_sel:[0,0,0,1]
	v_cvt_scalef32_pk_fp8_f32 v251, v244, v248, v254 op_sel:[0,0,0,1]
	s_add_u32 s90, s90, 0x1000
	s_addc_u32 s91, s91, 0
	global_store_dwordx2 v253, v[250:251], s[90:91] nt
	v_cvt_scalef32_pk_fp8_f32 v250, v221, v225, v254
	v_cvt_scalef32_pk_fp8_f32 v251, v237, v241, v254
	v_cvt_scalef32_pk_fp8_f32 v250, v229, v233, v254 op_sel:[0,0,0,1]
	v_cvt_scalef32_pk_fp8_f32 v251, v245, v249, v254 op_sel:[0,0,0,1]
	global_store_dwordx2 v253, v[250:251], s[90:91] offset:2048 nt
	s_add_i32 s98, s98, 1

; template <bool FP8, bool GATHER, class Epi, class Sched>
; __device__ __forceinline__ void gemm_phase(LAS unsigned char* lds, const Gemm g, const Sched& S, const Epi& E) {
;     ...
;         const bool has_next = S.next(ui + 1, nxt);
;         const bool cfull = FP8 ? true : (cur.full != 0);
;         nA = has_next ? (const char*)g.A + (size_t)nxt.pm * tstep : cA;
;         const char* nB = has_next ? (const char*)g.Bt + (size_t)nxt.e * estep + (size_t)nxt.pn * tstep : cB;
;     ...
; #pragma unroll
;         for (int a = 0; a < 2; ++a)
; #pragma unroll
;             for (int b = 0; b < 2; ++b)
; #pragma unroll
;                 for (int m = 0; m < 4; ++m)
; #pragma unroll
;                     for (int n = 0; n < 2; ++n) acc[a][b][m][n] = (f32x4){0.f, 0.f, 0.f, 0.f};
;         cur = nxt; cA = nA; cB = nB; ++ui;
.LBB0_864:
	s_ashr_i32 s17, s16, 31
	s_xor_b64 s[22:23], s[38:39], -1
	s_lshl_b64 s[20:21], s[16:17], 23
	s_add_u32 s2, s3, s20
	s_addc_u32 s17, s27, s21
	s_ashr_i32 s19, s18, 31
	s_lshl_b64 s[20:21], s[18:19], 19
	s_add_u32 s20, s2, s20
	s_addc_u32 s21, s17, s21
	s_and_b64 s[28:29], s[38:39], exec
	s_cselect_b32 s17, s21, s1
	s_cselect_b32 s19, s20, s0
	s_lshl_b32 s2, s80, 10
	s_add_u32 s25, s0, 0x100
	v_mov_b32_e32 v50, 0
	s_addc_u32 s28, s1, 0
	s_mov_b32 s29, -2
	v_add_u32_e32 v199, s2, v194
	v_mov_b32_e32 v51, v50
	v_mov_b32_e32 v52, v50
	v_mov_b32_e32 v53, v50
	v_mov_b32_e32 v58, v50
	v_mov_b32_e32 v59, v50
	v_mov_b32_e32 v60, v50
	v_mov_b32_e32 v61, v50
	v_mov_b32_e32 v66, v50
	v_mov_b32_e32 v67, v50
	v_mov_b32_e32 v68, v50
	v_mov_b32_e32 v69, v50
	v_mov_b32_e32 v74, v50
	v_mov_b32_e32 v75, v50
	v_mov_b32_e32 v76, v50
	v_mov_b32_e32 v77, v50
	v_mov_b32_e32 v82, v50
	v_mov_b32_e32 v83, v50
	v_mov_b32_e32 v84, v50
	v_mov_b32_e32 v85, v50
	v_mov_b32_e32 v90, v50
	v_mov_b32_e32 v91, v50
	v_mov_b32_e32 v92, v50
	v_mov_b32_e32 v93, v50
	v_mov_b32_e32 v98, v50
	v_mov_b32_e32 v99, v50
	v_mov_b32_e32 v100, v50
	v_mov_b32_e32 v101, v50
	v_mov_b32_e32 v106, v50
	v_mov_b32_e32 v107, v50
	v_mov_b32_e32 v108, v50
	v_mov_b32_e32 v109, v50
	v_mov_b32_e32 v54, v50
	v_mov_b32_e32 v55, v50
	v_mov_b32_e32 v56, v50
	v_mov_b32_e32 v57, v50
	v_mov_b32_e32 v62, v50
	v_mov_b32_e32 v63, v50
	v_mov_b32_e32 v64, v50
	v_mov_b32_e32 v65, v50
	v_mov_b32_e32 v70, v50
	v_mov_b32_e32 v71, v50
	v_mov_b32_e32 v72, v50
	v_mov_b32_e32 v73, v50
	v_mov_b32_e32 v78, v50
	v_mov_b32_e32 v79, v50
	v_mov_b32_e32 v80, v50
	v_mov_b32_e32 v81, v50
	v_mov_b32_e32 v86, v50
	v_mov_b32_e32 v87, v50
	v_mov_b32_e32 v88, v50
	v_mov_b32_e32 v89, v50
	v_mov_b32_e32 v94, v50
	v_mov_b32_e32 v95, v50
	v_mov_b32_e32 v96, v50
	v_mov_b32_e32 v97, v50
	v_mov_b32_e32 v102, v50
	v_mov_b32_e32 v103, v50
	v_mov_b32_e32 v104, v50
	v_mov_b32_e32 v105, v50
	v_mov_b32_e32 v110, v50
	v_mov_b32_e32 v111, v50
	v_mov_b32_e32 v112, v50
	v_mov_b32_e32 v113, v50
	v_mov_b32_e32 v114, v50
	v_mov_b32_e32 v115, v50
	v_mov_b32_e32 v116, v50
	v_mov_b32_e32 v117, v50
	v_mov_b32_e32 v122, v50
	v_mov_b32_e32 v123, v50
	v_mov_b32_e32 v124, v50
	v_mov_b32_e32 v125, v50
	v_mov_b32_e32 v130, v50
	v_mov_b32_e32 v131, v50
	v_mov_b32_e32 v132, v50
	v_mov_b32_e32 v133, v50
	v_mov_b32_e32 v138, v50
	v_mov_b32_e32 v139, v50
	v_mov_b32_e32 v140, v50
	v_mov_b32_e32 v141, v50
	v_mov_b32_e32 v146, v50
	v_mov_b32_e32 v147, v50
	v_mov_b32_e32 v148, v50
	v_mov_b32_e32 v149, v50
	v_mov_b32_e32 v154, v50
	v_mov_b32_e32 v155, v50
	v_mov_b32_e32 v156, v50
	v_mov_b32_e32 v157, v50
	v_mov_b32_e32 v162, v50
	v_mov_b32_e32 v163, v50
	v_mov_b32_e32 v164, v50
	v_mov_b32_e32 v165, v50
	v_mov_b32_e32 v170, v50
	v_mov_b32_e32 v171, v50
	v_mov_b32_e32 v172, v50
	v_mov_b32_e32 v173, v50
	v_mov_b32_e32 v118, v50
	v_mov_b32_e32 v119, v50
	v_mov_b32_e32 v120, v50
	v_mov_b32_e32 v121, v50
	v_mov_b32_e32 v126, v50
	v_mov_b32_e32 v127, v50
	v_mov_b32_e32 v128, v50
	v_mov_b32_e32 v129, v50
	v_mov_b32_e32 v134, v50
	v_mov_b32_e32 v135, v50
	v_mov_b32_e32 v136, v50
	v_mov_b32_e32 v137, v50
	v_mov_b32_e32 v142, v50
	v_mov_b32_e32 v143, v50
	v_mov_b32_e32 v144, v50
	v_mov_b32_e32 v145, v50
	v_mov_b32_e32 v150, v50
	v_mov_b32_e32 v151, v50
	v_mov_b32_e32 v152, v50
	v_mov_b32_e32 v153, v50
	v_mov_b32_e32 v158, v50
	v_mov_b32_e32 v159, v50
	v_mov_b32_e32 v160, v50
	v_mov_b32_e32 v161, v50
	v_mov_b32_e32 v166, v50
	v_mov_b32_e32 v167, v50
	v_mov_b32_e32 v168, v50
	v_mov_b32_e32 v169, v50
	v_mov_b32_e32 v174, v50
	v_mov_b32_e32 v175, v50
	v_mov_b32_e32 v176, v50
	v_mov_b32_e32 v177, v50
	s_add_i32 s32, s98, 7
	s_lshr_b32 s32, s32, 1
	s_mul_i32 s32, s32, s83
	s_add_i32 s32, s32, s84
	s_cmp_lt_u32 s32, 0x8000
	s_cselect_b32 s85, 1, 0
	s_cmp_lt_u32 s80, 2
	s_cselect_b32 s85, 0, s85
	s_cmp_gt_u32 s80, 3
	s_cselect_b32 s85, 0, s85
